# v19 + P2 loop keeps the packed-fp8 carry in v152-155 (8 v_mov per iteration removed from the barrier-to-ds_read path; copies only at loop entry/exit)
# speedup vs baseline: 1.0086x; 1.0086x over previous
.Lp2_top:
	ds_read_b128 v[158:161], v217
	ds_read_b128 v[162:165], v218
	ds_read_b128 v[166:169], v219
	ds_read_b128 v[170:173], v220
	ds_read_b128 v[148:151], v221
	ds_read_b128 v[144:147], v222
	ds_read_b128 v[140:143], v223
	ds_read_b128 v[136:139], v224
	ds_read_b128 v[174:177], v233
	ds_read_b128 v[178:181], v233 offset:1024
	ds_read_b128 v[182:185], v233 offset:2048
	ds_read_b128 v[186:189], v233 offset:3072
	ds_read_b128 v[190:193], v233 offset:4096
	ds_read_b128 v[194:197], v233 offset:5120
	ds_read_b128 v[234:237], v233 offset:6144
	ds_read_b128 v[238:241], v233 offset:7168
	s_add_i32 s4, s60, s61
	s_mov_b32 s46, s94
	s_add_i32 s94, s94, 1
	s_add_i32 s5, s4, 0x200
	s_add_i32 s16, s33, s61
	s_cmpk_eq_i32 s61, 0x1e00
	s_cselect_b32 s47, s90, s5
	s_cselect_b32 s97, s91, s16
	s_add_i32 s96, s47, 0x80
	s_mov_b32 m0, s82
	s_add_i32 s5, s4, 0x100180
	buffer_load_dwordx4 v214, s[8:11], s5 offen lds
	s_add_i32 s4, s4, 0x180180
	s_mov_b32 m0, s85
	s_add_i32 vcc_lo, s97, 0x80
	buffer_load_dwordx4 v214, s[8:11], s4 offen lds
	s_lshr_b32 s4, s94, 2
	s_mul_i32 s5, s4, s34
	s_add_i32 s16, s5, s2
	s_cmp_lt_i32 s4, s3
	s_cselect_b64 s[4:5], -1, 0
	s_and_b64 s[44:45], s[4:5], exec
	s_cselect_b32 s16, s16, 0
	s_bfe_u32 s17, s94, 0x10001
	s_or_b32 s17, s17, s83
	s_bfe_u32 s67, s16, 0x50007
	s_bfe_u32 s36, s16, 0x50002
	s_and_b32 s95, s16, 3
	s_cmpk_gt_i32 s16, 0xfff
	s_cselect_b64 s[44:45], -1, 0
	v_lshl_or_b32 v156, s17, 3, v216
	s_and_b64 s[16:17], s[44:45], exec
	s_cselect_b32 s16, s25, s21
	s_cselect_b32 s17, s24, s20
	s_lshl_b32 vcc_hi, s67, 23
	s_add_u32 s17, s17, vcc_hi
	s_addc_u32 s16, s16, 0
	s_lshl_b32 vcc_hi, s36, 18
	s_add_u32 s17, s17, vcc_hi
	s_addc_u32 vcc_hi, s16, 0
	s_lshl_b32 s16, s95, 9
	s_add_u32 s16, s17, s16
	v_and_or_b32 v204, s66, 2, v200
	s_addc_u32 s17, vcc_hi, 0
	v_lshlrev_b64 v[128:129], 11, v[204:205]
	v_lshl_add_u64 v[128:129], s[16:17], 0, v[128:129]
	v_lshlrev_b32_e32 v204, 4, v156
	v_lshl_add_u64 v[132:133], v[128:129], 0, v[204:205]
	global_load_dwordx4 v[128:131], v[132:133], off nt
	s_nop 0
	global_load_dwordx4 v[132:135], v[132:133], off offset:2048 nt
	s_waitcnt vmcnt(10)
	s_waitcnt lgkmcnt(8)
	s_barrier
	s_setprio 1
	s_waitcnt lgkmcnt(7)
	v_mfma_f32_16x16x32_bf16 v[124:127], v[158:161], v[174:177], v[124:127]
	s_waitcnt lgkmcnt(6)
	v_mfma_f32_16x16x32_bf16 v[124:127], v[162:165], v[178:181], v[124:127]
	v_mfma_f32_16x16x32_bf16 v[120:123], v[166:169], v[174:177], v[120:123]
	s_nop 0
	v_mfma_f32_16x16x32_bf16 v[120:123], v[170:173], v[178:181], v[120:123]
	s_waitcnt lgkmcnt(5)
	v_mfma_f32_16x16x32_bf16 v[116:119], v[158:161], v[182:185], v[116:119]
	s_waitcnt lgkmcnt(4)
	v_mfma_f32_16x16x32_bf16 v[116:119], v[162:165], v[186:189], v[116:119]
	v_mfma_f32_16x16x32_bf16 v[112:115], v[166:169], v[182:185], v[112:115]
	s_nop 0
	v_mfma_f32_16x16x32_bf16 v[112:115], v[170:173], v[186:189], v[112:115]
	s_waitcnt lgkmcnt(3)
	v_mfma_f32_16x16x32_bf16 v[108:111], v[158:161], v[190:193], v[108:111]
	s_waitcnt lgkmcnt(2)
	v_mfma_f32_16x16x32_bf16 v[108:111], v[162:165], v[194:197], v[108:111]
	v_mfma_f32_16x16x32_bf16 v[104:107], v[166:169], v[190:193], v[104:107]
	s_nop 0
	v_mfma_f32_16x16x32_bf16 v[104:107], v[170:173], v[194:197], v[104:107]
	s_waitcnt lgkmcnt(1)
	v_mfma_f32_16x16x32_bf16 v[100:103], v[158:161], v[234:237], v[100:103]
	s_waitcnt lgkmcnt(0)
	v_mfma_f32_16x16x32_bf16 v[100:103], v[162:165], v[238:241], v[100:103]
	v_mfma_f32_16x16x32_bf16 v[96:99], v[166:169], v[234:237], v[96:99]
	s_nop 0
	v_mfma_f32_16x16x32_bf16 v[96:99], v[170:173], v[238:241], v[96:99]
	s_setprio 0
	s_setprio 1
	v_mfma_f32_16x16x32_bf16 v[92:95], v[148:151], v[174:177], v[92:95]
	s_nop 0
	v_mfma_f32_16x16x32_bf16 v[92:95], v[144:147], v[178:181], v[92:95]
	v_mfma_f32_16x16x32_bf16 v[88:91], v[140:143], v[174:177], v[88:91]
	s_nop 0
	v_mfma_f32_16x16x32_bf16 v[88:91], v[136:139], v[178:181], v[88:91]
	v_mfma_f32_16x16x32_bf16 v[84:87], v[148:151], v[182:185], v[84:87]
	s_nop 0
	v_mfma_f32_16x16x32_bf16 v[84:87], v[144:147], v[186:189], v[84:87]
	v_mfma_f32_16x16x32_bf16 v[80:83], v[140:143], v[182:185], v[80:83]
	s_nop 0
	v_mfma_f32_16x16x32_bf16 v[80:83], v[136:139], v[186:189], v[80:83]
	v_mfma_f32_16x16x32_bf16 v[76:79], v[148:151], v[190:193], v[76:79]
	s_nop 0
	v_mfma_f32_16x16x32_bf16 v[76:79], v[144:147], v[194:197], v[76:79]
	v_mfma_f32_16x16x32_bf16 v[72:75], v[140:143], v[190:193], v[72:75]
	s_nop 0
	v_mfma_f32_16x16x32_bf16 v[72:75], v[136:139], v[194:197], v[72:75]
	v_mfma_f32_16x16x32_bf16 v[68:71], v[148:151], v[234:237], v[68:71]
	s_nop 0
	v_mfma_f32_16x16x32_bf16 v[68:71], v[144:147], v[238:241], v[68:71]
	v_mfma_f32_16x16x32_bf16 v[64:67], v[140:143], v[234:237], v[64:67]
	s_nop 0
	v_mfma_f32_16x16x32_bf16 v[64:67], v[136:139], v[238:241], v[64:67]
	s_setprio 0
	s_barrier
	ds_read_b128 v[174:177], v233 offset:16384
	ds_read_b128 v[178:181], v233 offset:17408
	ds_read_b128 v[182:185], v233 offset:18432
	ds_read_b128 v[186:189], v233 offset:19456
	ds_read_b128 v[190:193], v233 offset:20480
	ds_read_b128 v[194:197], v233 offset:21504
	ds_read_b128 v[234:237], v233 offset:22528
	ds_read_b128 v[238:241], v233 offset:23552
	s_mov_b32 m0, s65
	s_add_i32 s16, s97, 0x100000
	buffer_load_dwordx4 v215, s[12:15], s97 offen lds
	s_mov_b32 m0, s68
	s_nop 0
	buffer_load_dwordx4 v215, s[12:15], s16 offen lds
	s_add_i32 s16, s97, 0x10000
	s_mov_b32 m0, s69
	s_nop 0
	buffer_load_dwordx4 v215, s[12:15], s16 offen lds
	s_add_i32 s16, s97, 0x110000
	s_mov_b32 m0, s70
	s_nop 0
	buffer_load_dwordx4 v215, s[12:15], s16 offen lds
	s_mov_b32 m0, s64
	s_add_i32 s16, s47, 0x80000
	buffer_load_dwordx4 v214, s[8:11], s47 offen lds
	s_mov_b32 m0, s71
	s_nop 0
	buffer_load_dwordx4 v214, s[8:11], s16 offen lds
	s_waitcnt vmcnt(10)
	s_waitcnt lgkmcnt(6)
	s_barrier
	s_setprio 1
	s_waitcnt lgkmcnt(7)
	v_mfma_f32_16x16x32_bf16 v[60:63], v[158:161], v[174:177], v[60:63]
	s_waitcnt lgkmcnt(6)
	v_mfma_f32_16x16x32_bf16 v[60:63], v[162:165], v[178:181], v[60:63]
	v_mfma_f32_16x16x32_bf16 v[56:59], v[166:169], v[174:177], v[56:59]
	s_nop 0
	v_mfma_f32_16x16x32_bf16 v[56:59], v[170:173], v[178:181], v[56:59]
	s_waitcnt lgkmcnt(5)
	v_mfma_f32_16x16x32_bf16 v[52:55], v[158:161], v[182:185], v[52:55]
	s_waitcnt lgkmcnt(4)
	v_mfma_f32_16x16x32_bf16 v[52:55], v[162:165], v[186:189], v[52:55]
	v_mfma_f32_16x16x32_bf16 v[48:51], v[166:169], v[182:185], v[48:51]
	s_nop 0
	v_mfma_f32_16x16x32_bf16 v[48:51], v[170:173], v[186:189], v[48:51]
	s_waitcnt lgkmcnt(3)
	v_mfma_f32_16x16x32_bf16 v[44:47], v[158:161], v[190:193], v[44:47]
	s_waitcnt lgkmcnt(2)
	v_mfma_f32_16x16x32_bf16 v[44:47], v[162:165], v[194:197], v[44:47]
	v_mfma_f32_16x16x32_bf16 v[40:43], v[166:169], v[190:193], v[40:43]
	s_nop 0
	v_mfma_f32_16x16x32_bf16 v[40:43], v[170:173], v[194:197], v[40:43]
	s_waitcnt lgkmcnt(1)
	v_mfma_f32_16x16x32_bf16 v[36:39], v[158:161], v[234:237], v[36:39]
	s_waitcnt lgkmcnt(0)
	v_mfma_f32_16x16x32_bf16 v[36:39], v[162:165], v[238:241], v[36:39]
	v_mfma_f32_16x16x32_bf16 v[32:35], v[166:169], v[234:237], v[32:35]
	s_nop 0
	v_mfma_f32_16x16x32_bf16 v[32:35], v[170:173], v[238:241], v[32:35]
	s_setprio 0
	s_setprio 1
	v_mfma_f32_16x16x32_bf16 v[28:31], v[148:151], v[174:177], v[28:31]
	s_nop 0
	v_mfma_f32_16x16x32_bf16 v[28:31], v[144:147], v[178:181], v[28:31]
	v_mfma_f32_16x16x32_bf16 v[24:27], v[140:143], v[174:177], v[24:27]
	s_nop 0
	v_mfma_f32_16x16x32_bf16 v[24:27], v[136:139], v[178:181], v[24:27]
	v_mfma_f32_16x16x32_bf16 v[20:23], v[148:151], v[182:185], v[20:23]
	s_nop 0
	v_mfma_f32_16x16x32_bf16 v[20:23], v[144:147], v[186:189], v[20:23]
	v_mfma_f32_16x16x32_bf16 v[16:19], v[140:143], v[182:185], v[16:19]
	s_nop 0
	v_mfma_f32_16x16x32_bf16 v[16:19], v[136:139], v[186:189], v[16:19]
	v_mfma_f32_16x16x32_bf16 v[12:15], v[148:151], v[190:193], v[12:15]
	s_nop 0
	v_mfma_f32_16x16x32_bf16 v[12:15], v[144:147], v[194:197], v[12:15]
	v_mfma_f32_16x16x32_bf16 v[8:11], v[140:143], v[190:193], v[8:11]
	s_nop 0
	v_mfma_f32_16x16x32_bf16 v[8:11], v[136:139], v[194:197], v[8:11]
	v_mfma_f32_16x16x32_bf16 v[4:7], v[148:151], v[234:237], v[4:7]
	s_nop 0
	v_mfma_f32_16x16x32_bf16 v[4:7], v[144:147], v[238:241], v[4:7]
	v_mfma_f32_16x16x32_bf16 v[0:3], v[140:143], v[234:237], v[0:3]
	s_nop 0
	v_mfma_f32_16x16x32_bf16 v[0:3], v[136:139], v[238:241], v[0:3]
	s_setprio 0
	s_barrier
	ds_read_b128 v[136:139], v225
	ds_read_b128 v[140:143], v226
	ds_read_b128 v[144:147], v227
	ds_read_b128 v[148:151], v228
	ds_read_b128 v[158:161], v229
	ds_read_b128 v[162:165], v230
	ds_read_b128 v[166:169], v231
	ds_read_b128 v[170:173], v232
	ds_read_b128 v[174:177], v233 offset:32768
	ds_read_b128 v[178:181], v233 offset:33792
	ds_read_b128 v[182:185], v233 offset:34816
	ds_read_b128 v[186:189], v233 offset:35840
	ds_read_b128 v[190:193], v233 offset:36864
	ds_read_b128 v[194:197], v233 offset:37888
	ds_read_b128 v[234:237], v233 offset:38912
	ds_read_b128 v[238:241], v233 offset:39936
	s_mov_b32 m0, s72
	s_add_i32 s16, s47, 0x100000
	buffer_load_dwordx4 v214, s[8:11], s16 offen lds
	s_add_i32 s16, s47, 0x180000
	s_mov_b32 m0, s73
	s_nop 0
	buffer_load_dwordx4 v214, s[8:11], s16 offen lds
	s_waitcnt vmcnt(10)
	s_waitcnt lgkmcnt(8)
	s_barrier
	s_setprio 1
	s_waitcnt lgkmcnt(7)
	v_mfma_f32_16x16x32_bf16 v[124:127], v[136:139], v[174:177], v[124:127]
	s_waitcnt lgkmcnt(6)
	v_mfma_f32_16x16x32_bf16 v[124:127], v[140:143], v[178:181], v[124:127]
	v_mfma_f32_16x16x32_bf16 v[120:123], v[144:147], v[174:177], v[120:123]
	s_nop 0
	v_mfma_f32_16x16x32_bf16 v[120:123], v[148:151], v[178:181], v[120:123]
	s_waitcnt lgkmcnt(5)
	v_mfma_f32_16x16x32_bf16 v[116:119], v[136:139], v[182:185], v[116:119]
	s_waitcnt lgkmcnt(4)
	v_mfma_f32_16x16x32_bf16 v[116:119], v[140:143], v[186:189], v[116:119]
	v_mfma_f32_16x16x32_bf16 v[112:115], v[144:147], v[182:185], v[112:115]
	s_nop 0
	v_mfma_f32_16x16x32_bf16 v[112:115], v[148:151], v[186:189], v[112:115]
	s_waitcnt lgkmcnt(3)
	v_mfma_f32_16x16x32_bf16 v[108:111], v[136:139], v[190:193], v[108:111]
	s_waitcnt lgkmcnt(2)
	v_mfma_f32_16x16x32_bf16 v[108:111], v[140:143], v[194:197], v[108:111]
	v_mfma_f32_16x16x32_bf16 v[104:107], v[144:147], v[190:193], v[104:107]
	s_nop 0
	v_mfma_f32_16x16x32_bf16 v[104:107], v[148:151], v[194:197], v[104:107]
	s_waitcnt lgkmcnt(1)
	v_mfma_f32_16x16x32_bf16 v[100:103], v[136:139], v[234:237], v[100:103]
	s_waitcnt lgkmcnt(0)
	v_mfma_f32_16x16x32_bf16 v[100:103], v[140:143], v[238:241], v[100:103]
	v_mfma_f32_16x16x32_bf16 v[96:99], v[144:147], v[234:237], v[96:99]
	s_nop 0
	v_mfma_f32_16x16x32_bf16 v[96:99], v[148:151], v[238:241], v[96:99]
	s_setprio 0
	s_setprio 1
	v_mfma_f32_16x16x32_bf16 v[92:95], v[158:161], v[174:177], v[92:95]
	s_nop 0
	v_mfma_f32_16x16x32_bf16 v[92:95], v[162:165], v[178:181], v[92:95]
	v_mfma_f32_16x16x32_bf16 v[88:91], v[166:169], v[174:177], v[88:91]
	s_nop 0
	v_mfma_f32_16x16x32_bf16 v[88:91], v[170:173], v[178:181], v[88:91]
	v_mfma_f32_16x16x32_bf16 v[84:87], v[158:161], v[182:185], v[84:87]
	s_nop 0
	v_mfma_f32_16x16x32_bf16 v[84:87], v[162:165], v[186:189], v[84:87]
	v_mfma_f32_16x16x32_bf16 v[80:83], v[166:169], v[182:185], v[80:83]
	s_nop 0
	v_mfma_f32_16x16x32_bf16 v[80:83], v[170:173], v[186:189], v[80:83]
	v_mfma_f32_16x16x32_bf16 v[76:79], v[158:161], v[190:193], v[76:79]
	s_nop 0
	v_mfma_f32_16x16x32_bf16 v[76:79], v[162:165], v[194:197], v[76:79]
	v_mfma_f32_16x16x32_bf16 v[72:75], v[166:169], v[190:193], v[72:75]
	s_nop 0
	v_mfma_f32_16x16x32_bf16 v[72:75], v[170:173], v[194:197], v[72:75]
	v_mfma_f32_16x16x32_bf16 v[68:71], v[158:161], v[234:237], v[68:71]
	s_nop 0
	v_mfma_f32_16x16x32_bf16 v[68:71], v[162:165], v[238:241], v[68:71]
	v_mfma_f32_16x16x32_bf16 v[64:67], v[166:169], v[234:237], v[64:67]
	s_nop 0
	v_mfma_f32_16x16x32_bf16 v[64:67], v[170:173], v[238:241], v[64:67]
	s_setprio 0
	s_barrier
	ds_read_b128 v[174:177], v233 offset:49152
	ds_read_b128 v[178:181], v233 offset:50176
	ds_read_b128 v[182:185], v233 offset:51200
	ds_read_b128 v[186:189], v233 offset:52224
	ds_read_b128 v[190:193], v233 offset:53248
	ds_read_b128 v[194:197], v233 offset:54272
	ds_read_b128 v[234:237], v233 offset:55296
	ds_read_b128 v[238:241], v233 offset:56320
	s_mov_b32 m0, s76
	s_add_i32 s16, s97, 0x100080
	buffer_load_dwordx4 v215, s[12:15], vcc_lo offen lds
	s_mov_b32 m0, s77
	s_add_i32 s47, s47, 0x80080
	buffer_load_dwordx4 v215, s[12:15], s16 offen lds
	s_add_i32 s16, s97, 0x10080
	s_mov_b32 m0, s80
	s_add_i32 s97, s97, 0x110080
	buffer_load_dwordx4 v215, s[12:15], s16 offen lds
	s_mov_b32 m0, s81
	s_nop 0
	buffer_load_dwordx4 v215, s[12:15], s97 offen lds
	s_mov_b32 m0, s78
	s_nop 0
	buffer_load_dwordx4 v214, s[8:11], s96 offen lds
	s_mov_b32 m0, s79
	s_nop 0
	buffer_load_dwordx4 v214, s[8:11], s47 offen lds
	s_bitcmp0_b32 s46, 0
	s_mov_b32 s98, 0xffff
	s_cselect_b32 s98, 0xffff0000, s98
	s_waitcnt vmcnt(8)
	s_waitcnt lgkmcnt(6)
	s_barrier
	s_setprio 1
	s_waitcnt lgkmcnt(7)
	v_mfma_f32_16x16x32_bf16 v[60:63], v[136:139], v[174:177], v[60:63]
	s_waitcnt lgkmcnt(6)
	v_mfma_f32_16x16x32_bf16 v[60:63], v[140:143], v[178:181], v[60:63]
	v_mfma_f32_16x16x32_bf16 v[56:59], v[144:147], v[174:177], v[56:59]
	v_mul_f32_e32 v128, 0x42800000, v128
	v_mfma_f32_16x16x32_bf16 v[56:59], v[148:151], v[178:181], v[56:59]
	v_mul_f32_e32 v130, 0x42800000, v130
	s_waitcnt lgkmcnt(5)
	v_mfma_f32_16x16x32_bf16 v[52:55], v[136:139], v[182:185], v[52:55]
	s_waitcnt lgkmcnt(4)
	v_mfma_f32_16x16x32_bf16 v[52:55], v[140:143], v[186:189], v[52:55]
	v_mfma_f32_16x16x32_bf16 v[48:51], v[144:147], v[182:185], v[48:51]
	v_mul_f32_e32 v132, 0x42800000, v132
	v_mfma_f32_16x16x32_bf16 v[48:51], v[148:151], v[186:189], v[48:51]
	v_mul_f32_e32 v134, 0x42800000, v134
	s_waitcnt lgkmcnt(3)
	v_mfma_f32_16x16x32_bf16 v[44:47], v[136:139], v[190:193], v[44:47]
	s_waitcnt lgkmcnt(2)
	v_mfma_f32_16x16x32_bf16 v[44:47], v[140:143], v[194:197], v[44:47]
	v_mfma_f32_16x16x32_bf16 v[40:43], v[144:147], v[190:193], v[40:43]
	v_mul_f32_e32 v129, 0x42800000, v129
	v_mfma_f32_16x16x32_bf16 v[40:43], v[148:151], v[194:197], v[40:43]
	v_mul_f32_e32 v131, 0x42800000, v131
	s_waitcnt lgkmcnt(1)
	v_mfma_f32_16x16x32_bf16 v[36:39], v[136:139], v[234:237], v[36:39]
	s_waitcnt lgkmcnt(0)
	v_mfma_f32_16x16x32_bf16 v[36:39], v[140:143], v[238:241], v[36:39]
	v_mfma_f32_16x16x32_bf16 v[32:35], v[144:147], v[234:237], v[32:35]
	v_mul_f32_e32 v133, 0x42800000, v133
	v_mfma_f32_16x16x32_bf16 v[32:35], v[148:151], v[238:241], v[32:35]
	v_mul_f32_e32 v135, 0x42800000, v135
	s_setprio 0
	s_setprio 1
	v_mfma_f32_16x16x32_bf16 v[28:31], v[158:161], v[174:177], v[28:31]
	v_cvt_pk_fp8_f32 v204, v128, v132
	v_mfma_f32_16x16x32_bf16 v[28:31], v[162:165], v[178:181], v[28:31]
	v_mfma_f32_16x16x32_bf16 v[24:27], v[166:169], v[174:177], v[24:27]
	v_cvt_pk_fp8_f32 v204, v128, v132 op_sel:[0,0,1]
	v_mfma_f32_16x16x32_bf16 v[24:27], v[170:173], v[178:181], v[24:27]
	v_mfma_f32_16x16x32_bf16 v[20:23], v[158:161], v[182:185], v[20:23]
	v_cvt_pk_fp8_f32 v250, v129, v133
	v_mfma_f32_16x16x32_bf16 v[20:23], v[162:165], v[186:189], v[20:23]
	v_mfma_f32_16x16x32_bf16 v[16:19], v[166:169], v[182:185], v[16:19]
	v_cvt_pk_fp8_f32 v250, v129, v133 op_sel:[0,0,1]
	v_mfma_f32_16x16x32_bf16 v[16:19], v[170:173], v[186:189], v[16:19]
	v_mfma_f32_16x16x32_bf16 v[12:15], v[158:161], v[190:193], v[12:15]
	v_cvt_pk_fp8_f32 v251, v130, v134
	v_mfma_f32_16x16x32_bf16 v[12:15], v[162:165], v[194:197], v[12:15]
	v_bfi_b32 v152, s98, v204, v152
	v_mfma_f32_16x16x32_bf16 v[8:11], v[166:169], v[190:193], v[8:11]
	v_cvt_pk_fp8_f32 v251, v130, v134 op_sel:[0,0,1]
	v_mfma_f32_16x16x32_bf16 v[8:11], v[170:173], v[194:197], v[8:11]
	v_bfi_b32 v153, s98, v250, v153
	v_mfma_f32_16x16x32_bf16 v[4:7], v[158:161], v[234:237], v[4:7]
	v_cvt_pk_fp8_f32 v252, v131, v135
	v_mfma_f32_16x16x32_bf16 v[4:7], v[162:165], v[238:241], v[4:7]
	v_bfi_b32 v154, s98, v251, v154
	v_mfma_f32_16x16x32_bf16 v[0:3], v[166:169], v[234:237], v[0:3]
	v_cvt_pk_fp8_f32 v252, v131, v135 op_sel:[0,0,1]
	v_mfma_f32_16x16x32_bf16 v[0:3], v[170:173], v[238:241], v[0:3]
	v_bfi_b32 v155, s98, v252, v155
	s_setprio 0
	s_barrier
	s_bitcmp0_b32 s46, 0
	s_mov_b64 s[46:47], -1
	s_cbranch_scc0 .LBB0_345
	s_andn2_b64 vcc, exec, s[4:5]
	s_cbranch_vccnz .LBB0_345
	s_lshl_b32 s4, s67, 10
	s_lshl_b32 s5, s95, 8
	s_or_b32 s16, s4, s5
	s_and_b64 s[4:5], s[44:45], exec
	s_cselect_b32 s4, 8, 0
	v_lshlrev_b32_e32 v128, 3, v156
	s_or_b32 s4, s4, s16
	v_and_b32_e32 v128, 0xf0, v128
	v_or_b32_e32 v128, s4, v128
	v_or_b32_e32 v204, v128, v202
	v_lshlrev_b64 v[128:129], 12, v[204:205]
	v_lshl_add_u64 v[128:129], s[6:7], 0, v[128:129]
	s_lshl_b32 s36, s36, 7
	v_lshl_add_u64 v[128:129], v[128:129], 0, s[36:37]
	v_lshl_add_u64 v[128:129], v[128:129], 0, v[200:201]
	v_add_co_u32_e32 v130, vcc, 0x1000, v128
	global_store_dword v[128:129], v152, off
	s_nop 0
	v_addc_co_u32_e32 v131, vcc, 0, v129, vcc
	global_store_dword v[130:131], v153, off
	v_add_co_u32_e32 v130, vcc, 0x2000, v128
	s_nop 1
	v_addc_co_u32_e32 v131, vcc, 0, v129, vcc
	v_add_co_u32_e32 v128, vcc, 0x3000, v128
	global_store_dword v[130:131], v154, off
	s_nop 0
	v_addc_co_u32_e32 v129, vcc, 0, v129, vcc
	global_store_dword v[128:129], v155, off
	s_branch .LBB0_345
.LBB0_345:
.LBB0_346:
	s_addk_i32 s61, 0x100
	s_add_i32 s66, s66, 2
	s_cmpk_eq_i32 s61, 0x1f00
	s_cbranch_scc0 .Lp2_top
	v_mov_b32_e32 v204, v152
	v_mov_b32_e32 v234, v153
	v_mov_b32_e32 v235, v154
	v_mov_b32_e32 v236, v155
